# attn_k: static s_setprio 1 for the older waves 0-3 (the critical half after the 5:3 tile rebalance), on top of reduce_slabs rewrite
# speedup vs baseline: 1.0217x; 1.0002x over previous
_Z6attn_kPKDF16_S0_S0_PDF16_:
	v_readfirstlane_b32 s13, v0
	s_movk_i32 s14, 0x200
	s_nop 2
	s_cmpk_lt_u32 s13, 0x100
	s_cselect_b32 s14, 0x380, s14
	s_add_i32 s15, s14, 0x100
	v_readfirstlane_b32 s13, v0
	s_load_dwordx8 s[4:11], s[0:1], 0x0
	s_lshr_b32 s1, s2, 2
	s_and_b32 s0, s2, 7
	s_and_b32 s1, s1, 8
	s_or_b32 s0, s1, s0
	s_lshr_b32 s3, s2, 6
	s_lshl_b32 s1, s3, 8
	s_lshl_b32 s12, s0, 6
	s_lshl_b32 s0, s0, 7
	s_waitcnt lgkmcnt(0)
	s_add_u32 s6, s6, s0
	v_lshlrev_b32_e32 v1, 4, v0
	s_addc_u32 s7, s7, 0
	v_and_b32_e32 v180, 0x70, v1
	v_mov_b32_e32 v181, 0
	v_lshrrev_b32_e32 v36, 3, v0
	v_or_b32_e32 v22, 0x200, v0
	v_lshl_add_u64 v[10:11], s[6:7], 0, v[180:181]
	v_or_b32_e32 v180, s1, v36
	v_lshrrev_b32_e32 v37, 3, v22
	v_or_b32_e32 v32, 0x400, v0
	v_lshlrev_b64 v[2:3], 11, v[180:181]
	v_or_b32_e32 v180, s1, v37
	v_lshrrev_b32_e32 v38, 3, v32
	v_or_b32_e32 v33, 0x600, v0
	v_lshl_add_u64 v[12:13], v[10:11], 0, v[2:3]
	v_lshlrev_b64 v[2:3], 11, v[180:181]
	v_or_b32_e32 v180, s1, v38
	v_lshrrev_b32_e32 v39, 3, v33
	v_lshl_add_u64 v[14:15], v[10:11], 0, v[2:3]
	global_load_dwordx4 v[2:5], v[12:13], off
	global_load_dwordx4 v[6:9], v[14:15], off
	v_lshlrev_b64 v[12:13], 11, v[180:181]
	v_or_b32_e32 v180, s1, v39
	v_and_b32_e32 v40, 31, v0
	s_lshl_b32 s1, s3, 10
	v_lshl_add_u64 v[18:19], v[10:11], 0, v[12:13]
	v_lshlrev_b64 v[12:13], 11, v[180:181]
	s_or_b32 s1, s12, s1
	v_lshlrev_b32_e32 v180, 4, v40
	v_lshrrev_b32_e32 v41, 5, v0
	v_lshl_add_u64 v[20:21], v[10:11], 0, v[12:13]
	global_load_dwordx4 v[10:13], v[18:19], off
	global_load_dwordx4 v[14:17], v[20:21], off
	v_lshl_add_u64 v[30:31], s[8:9], 0, v[180:181]
	v_or_b32_e32 v180, s1, v41
	v_lshrrev_b32_e32 v42, 5, v22
	v_lshlrev_b64 v[18:19], 9, v[180:181]
	v_or_b32_e32 v180, s1, v42
	v_lshrrev_b32_e32 v43, 5, v32
	v_lshl_add_u64 v[26:27], v[30:31], 0, v[18:19]
	v_lshlrev_b64 v[18:19], 9, v[180:181]
	v_or_b32_e32 v180, s1, v43
	v_lshl_add_u64 v[28:29], v[30:31], 0, v[18:19]
	global_load_dwordx4 v[18:21], v[26:27], off
	global_load_dwordx4 v[22:25], v[28:29], off
	v_lshlrev_b64 v[26:27], 9, v[180:181]
	v_lshl_add_u64 v[26:27], v[30:31], 0, v[26:27]
	global_load_dwordx4 v[26:29], v[26:27], off
	v_lshrrev_b32_e32 v45, 6, v0
	s_lshl_b32 s2, s2, 7
	v_lshrrev_b32_e32 v44, 5, v33
	s_and_b32 s6, s2, 0xc00
	v_lshlrev_b32_e32 v47, 5, v45
	v_or_b32_e32 v180, s1, v44
	v_or_b32_e32 v34, s6, v47
	s_lshl_b32 s7, s3, 12
	v_lshlrev_b64 v[32:33], 9, v[180:181]
	v_or3_b32 v180, s7, v40, v34
	v_lshlrev_b64 v[34:35], 11, v[180:181]
	v_bfe_u32 v46, v0, 5, 1
	s_mov_b32 s1, 0
	v_lshl_add_u64 v[34:35], s[4:5], 0, v[34:35]
	v_lshl_add_u64 v[34:35], v[34:35], 0, s[0:1]
	v_lshlrev_b32_e32 v180, 4, v46
	v_lshl_add_u64 v[30:31], v[30:31], 0, v[32:33]
	v_lshl_add_u64 v[34:35], v[34:35], 0, v[180:181]
	global_load_dwordx4 v[30:33], v[30:31], off
	s_nop 0
	global_load_dwordx4 v[120:123], v[34:35], off
	global_load_dwordx4 v[124:127], v[34:35], off offset:32
	global_load_dwordx4 v[116:119], v[34:35], off offset:64
	global_load_dwordx4 v[112:115], v[34:35], off offset:96
	s_movk_i32 s2, 0x70
	v_bitop3_b32 v1, v1, s2, v0 bitop3:0x48
	v_lshl_or_b32 v35, v36, 7, v1
	v_lshl_or_b32 v36, v37, 7, v1
	v_lshl_or_b32 v37, v38, 7, v1
	v_lshl_or_b32 v1, v39, 7, v1
	s_add_u32 s2, s4, s0
	v_mul_u32_u24_e32 v34, 0x1200, v45
	s_addc_u32 s3, s5, 0
	v_lshl_add_u64 v[182:183], s[2:3], 0, v[180:181]
	s_movk_i32 s2, 0x90
	s_waitcnt vmcnt(11)
	ds_write_b128 v35, v[2:5]
	s_waitcnt vmcnt(10)
	ds_write_b128 v36, v[6:9]
	s_waitcnt vmcnt(9)
	ds_write_b128 v37, v[10:13]
	s_waitcnt vmcnt(8)
	ds_write_b128 v1, v[14:17]
	v_bitop3_b32 v1, v41, v0, 31 bitop3:0x78
	v_lshlrev_b32_e32 v1, 4, v1
	v_lshl_or_b32 v2, v41, 9, v1
	v_lshlrev_b32_e32 v3, 1, v0
	v_lshrrev_b32_e32 v4, 1, v0
	v_and_b32_e32 v3, 8, v3
	v_and_b32_e32 v4, 4, v4
	s_waitcnt vmcnt(7)
	ds_write_b128 v2, v[18:21] offset:32768
	v_lshl_or_b32 v2, v42, 9, v1
	s_waitcnt vmcnt(6)
	ds_write_b128 v2, v[22:25] offset:32768
	v_lshl_or_b32 v2, v43, 9, v1
	s_waitcnt vmcnt(5)
	ds_write_b128 v2, v[26:29] offset:32768
	v_and_b32_e32 v2, 19, v0
	v_or3_b32 v2, v3, v2, v4
	v_lshrrev_b32_e32 v4, 1, v2
	v_lshlrev_b32_e32 v3, 7, v2
	v_bfe_u32 v2, v2, 1, 3
	v_bitop3_b32 v4, v46, v4, 7 bitop3:0x78
	v_lshl_or_b32 v186, v4, 4, v3
	v_bitop3_b32 v4, v46, v2, 2 bitop3:0x36
	v_lshl_or_b32 v187, v4, 4, v3
	v_bitop3_b32 v4, v46, v2, 4 bitop3:0x36
	v_bitop3_b32 v2, v46, v2, 6 bitop3:0x36
	v_lshl_or_b32 v188, v4, 4, v3
	v_lshl_or_b32 v189, v2, 4, v3
	v_lshlrev_b32_e32 v2, 9, v40
	v_and_b32_e32 v3, 15, v0
	v_bitop3_b32 v4, v46, v0, 15 bitop3:0x78
	v_lshl_or_b32 v190, v4, 4, v2
	v_bitop3_b32 v4, v46, v3, 2 bitop3:0x36
	v_lshl_or_b32 v191, v4, 4, v2
	v_bitop3_b32 v4, v46, v3, 4 bitop3:0x36
	v_lshl_or_b32 v192, v4, 4, v2
	v_bitop3_b32 v4, v46, v3, 6 bitop3:0x36
	v_lshl_or_b32 v193, v4, 4, v2
	v_bitop3_b32 v4, v46, v3, 8 bitop3:0x36
	v_lshl_or_b32 v194, v4, 4, v2
	v_bitop3_b32 v4, v46, v3, 10 bitop3:0x36
	v_lshl_or_b32 v195, v4, 4, v2
	v_bitop3_b32 v4, v46, v3, 12 bitop3:0x36
	v_bitop3_b32 v3, v46, v3, 14 bitop3:0x36
	v_lshl_or_b32 v197, v3, 4, v2
	v_mbcnt_lo_u32_b32 v3, -1, 0
	v_mbcnt_hi_u32_b32 v3, -1, v3
	v_and_b32_e32 v5, 64, v3
	v_lshl_or_b32 v196, v4, 4, v2
	v_xor_b32_e32 v4, 32, v3
	v_add_u32_e32 v5, 64, v5
	v_cmp_lt_i32_e32 vcc, v4, v5
	v_or_b32_e32 v2, 0x10000, v34
	v_lshl_or_b32 v1, v44, 9, v1
	v_cndmask_b32_e32 v3, v3, v4, vcc
	v_lshlrev_b32_e32 v198, 2, v3
	v_mad_u32_u24 v3, v40, s2, v2
	v_bfe_u32 v4, v0, 3, 3
	v_and_b32_e32 v0, 7, v0
	s_add_u32 s2, s10, s0
	v_lshlrev_b32_e32 v180, 4, v0
	s_addc_u32 s3, s11, 0
	v_or_b32_e32 v5, 8, v4
	s_or_b32 s0, s7, s6
	s_waitcnt vmcnt(4)
	ds_write_b128 v1, v[30:33] offset:32768
	v_lshlrev_b32_e32 v1, 3, v46
	s_waitcnt lgkmcnt(0)
	s_barrier
	s_cmpk_lt_u32 s13, 0x100
	s_cbranch_scc0 .Lattn_noprio
	s_setprio 1
.Lattn_noprio:
	s_waitcnt vmcnt(3)
	s_waitcnt vmcnt(2)
	s_waitcnt vmcnt(1)
	s_waitcnt vmcnt(0)
	v_or_b32_e32 v0, v2, v180
	v_mul_u32_u24_e32 v2, 0x90, v4
	v_mul_u32_u24_e32 v5, 0x90, v5
	v_or_b32_e32 v6, s0, v47
	s_movk_i32 s0, 0x100
	v_mov_b64_e32 v[96:97], v[120:121]
	v_mov_b64_e32 v[100:101], v[124:125]
	v_mov_b64_e32 v[104:105], v[116:117]
	v_mov_b64_e32 v[108:109], v[112:113]
	v_lshl_add_u64 v[184:185], s[2:3], 0, v[180:181]
	v_or3_b32 v199, v6, v40, s0
	v_or_b32_e32 v200, v6, v4
	s_mov_b32 s0, 0xf149f2ca
	v_add_u32_e32 v201, v3, v1
	v_add_u32_e32 v202, v0, v2
	v_add_u32_e32 v203, v0, v5
	v_mov_b64_e32 v[98:99], v[122:123]
	v_mov_b64_e32 v[102:103], v[126:127]
	v_mov_b64_e32 v[106:107], v[118:119]
	v_mov_b64_e32 v[110:111], v[114:115]
	s_branch .LBB5_2
